# grid barrier, first use: the 16 per-XCD arrival counts are loaded back to back instead of one dependent round trip each
# speedup vs baseline: 1.0226x; 1.0027x over previous
; __device__ __forceinline__ unsigned xb_ld(unsigned* p)              { return __hip_atomic_load(p, __ATOMIC_RELAXED, __HIP_MEMORY_SCOPE_AGENT); }
; __device__ __forceinline__ void xcd_barrier_complete(unsigned* bar, unsigned x, unsigned& nloc, unsigned& nx) {
;     const unsigned G = gridDim.x * gridDim.y * gridDim.z;
;     unsigned sum, cnt, mine, sp = 0u;
;     for (;;) {
;         sum = 0u; cnt = 0u; mine = 0u;
; #pragma unroll
;         for (unsigned j = 0; j < 16; ++j) { const unsigned c = xb_ld(&bar[XB_XCNT(j)]); sum += c; cnt += (c > 0u) ? 1u : 0u; mine = (j == x) ? c : mine; }
;         if (sum == G) break;
;         __builtin_amdgcn_s_sleep(1);
;         if ((++sp & 255u) == 0u) { if (xb_ld(&bar[XB_TMO])) break; if (sp > XB_SPIN_CAP) { atomicAdd(&bar[XB_TMO], 1u); break; } }
;     }
;     nloc = mine > 0u ? mine : 1u; nx = cnt > 0u ? cnt : 1u;
; }
.LBB0_714:
	v_readlane_b32 s6, v253, 42
	v_readlane_b32 s7, v253, 43
	s_mov_b64 s[42:43], -1
	s_mov_b64 s[44:45], -1
	s_nop 2
	global_load_dword v2, v3, s[6:7] sc1
	global_load_dword v4, v3, s[6:7] offset:256 sc1
	global_load_dword v5, v3, s[6:7] offset:512 sc1
	global_load_dword v6, v3, s[6:7] offset:768 sc1
	global_load_dword v7, v3, s[6:7] offset:1024 sc1
	global_load_dword v8, v3, s[6:7] offset:1280 sc1
	global_load_dword v9, v3, s[6:7] offset:1536 sc1
	global_load_dword v10, v3, s[6:7] offset:1792 sc1
	global_load_dword v11, v3, s[6:7] offset:2048 sc1
	global_load_dword v12, v3, s[6:7] offset:2304 sc1
	global_load_dword v13, v3, s[6:7] offset:2560 sc1
	global_load_dword v14, v3, s[6:7] offset:2816 sc1
	global_load_dword v15, v3, s[6:7] offset:3072 sc1
	global_load_dword v16, v3, s[6:7] offset:3328 sc1
	global_load_dword v17, v3, s[6:7] offset:3584 sc1
	global_load_dword v18, v3, s[6:7] offset:3840 sc1
	s_waitcnt vmcnt(0)
	v_add_u32_e32 v19, v4, v2
	v_add_u32_e32 v19, v19, v5
	v_add_u32_e32 v19, v19, v6
	v_add_u32_e32 v19, v19, v7
	v_add_u32_e32 v19, v19, v8
	v_add_u32_e32 v19, v19, v9
	v_add_u32_e32 v19, v19, v10
	v_add_u32_e32 v19, v19, v11
	v_add_u32_e32 v19, v19, v12
	v_add_u32_e32 v19, v19, v13
	v_add_u32_e32 v19, v19, v14
	v_add_u32_e32 v19, v19, v15
	v_add_u32_e32 v19, v19, v16
	v_add_u32_e32 v19, v19, v17
	v_add_u32_e32 v19, v19, v18
	v_cmp_eq_u32_e32 vcc, s15, v19
	s_cbranch_vccnz .LBB0_713
	s_and_b32 s6, s16, 0xff
	s_cmp_eq_u32 s6, 0
	s_mov_b64 s[6:7], -1
	s_sleep 1
	s_cbranch_scc1 .LBB0_718
	s_and_b64 vcc, exec, s[6:7]
	s_cbranch_vccz .LBB0_713
